# sel: a block's next-triple DMA issue interleaved into the idle issue slots between the tile's four score MFMAs (block-head issue only when the wave has no tile there)
# speedup vs baseline: 1.0031x; 1.0008x over previous
; __device__ __forceinline__ unsigned lds_addr(const LAS void* p) { return (unsigned)(size_t)p; }
; #define RD16(dst, base, off) asm volatile("ds_read_b128 %0, %1 offset:%2" : "=&v"(dst) : "v"(base), "i"(off) : "memory")
; #define LGKM_W(n) asm volatile("s_waitcnt lgkmcnt(" #n ")" ::: "memory"); SBAR()
; #define QK8_MM(T_) do { i32x8a kf; kf.lo = lo[T_]; kf.hi = hi[T_]; s[T_] = __builtin_amdgcn_mfma_scale_f32_16x16x128_f8f6f4(kf, g.q8, (f32x4){c0, c0, c0, c0}, 0, 0, 0, 0x7f7f7f7f, 0, 0x7c7c7c7c); } while (0)
; __device__ __forceinline__ void qk8_tile_c(f32x4 (&s)[4], const GS8& g, const unsigned kb  , const float c0  ) {
;     i32x4a lo[4], hi[4];
;     RD16(lo[0], kb, 0); RD16(hi[0], kb, 16); RD16(lo[1], kb, 16 * K8ST); RD16(hi[1], kb, 16 * K8ST + 16);
;     RD16(lo[2], kb, 32 * K8ST); RD16(hi[2], kb, 32 * K8ST + 16); RD16(lo[3], kb, 48 * K8ST); RD16(hi[3], kb, 48 * K8ST + 16);
;     ...
;     LGKM_W(6); QK8_MM(0); LGKM_W(4); QK8_MM(1); LGKM_W(2); QK8_MM(2); LGKM_W(0); QK8_MM(3);
;     ...
; }
; template <bool DUMMY> __device__ __forceinline__ void sel_phase(Frame& F) {
;     ...
;                 const unsigned a0 = byte & 0xfu, a1 = byte >> 4;
;                 if (byte == 0u) continue;
;                 const bool selA = ((a0 >> (c >> 2)) & 1u) != 0u, selB = ((a1 >> (c >> 2)) & 1u) != 0u;
;                 const float NINF = -__builtin_inff();
;                 const int kb = jc * 64; const bool diag = (jc == cur); f32x4 s0[4], s1[4];
;                 const float bA = selA ? 0.f : NINF, bB = selB ? 0.f : NINF;
;                 if (a0 != 0u) {
;                     const float rf = sm8_ref(g0);
;                     VT8Frag vf; qk8_tile_c(s0, g0, lds_addr(sb) + (unsigned)klane, bA + (5.f - rf)); pv8_issue(vf, lds_addr(sb + K8TB) + (unsigned)vtlane);
.Lsel_tile:
	ds_read_b128 v[84:87], v208 offset:0
	ds_read_b128 v[88:91], v208 offset:16
	ds_read_b128 v[92:95], v208 offset:0x900
	ds_read_b128 v[96:99], v208 offset:0x910
	ds_read_b128 v[118:121], v208 offset:0x1200
	ds_read_b128 v[122:125], v208 offset:0x1210
	s_and_b32 vcc_lo, s45, 15
	s_cbranch_scc0 .Lsel_g1_pre
	v_and_b32_e32 v18, s45, v154
	v_cmp_eq_u32_e32 vcc, 0, v18
	s_lshr_b32 s44, s66, s36
	s_and_b32 s44, s44, 0xff
	v_cndmask_b32_e32 v210, v216, v181, vcc
	v_mov_b32_e32 v211, v210
	v_mov_b32_e32 v212, v210
	v_mov_b32_e32 v213, v210
	ds_read_b128 v[126:129], v208 offset:0x1b00
	ds_read_b128 v[130:133], v208 offset:0x1b10
	s_bitcmp1_b32 s99, s37
	s_cbranch_scc1 .Lsel_qk_dma_g0
	s_waitcnt lgkmcnt(6)
	v_mfma_scale_f32_16x16x128_f8f6f4 v[84:87], v[84:91], v[0:7], v[210:213], v178, v177 op_sel_hi:[0,0,0]
	ds_read_b128 v[134:137], v207 offset:0
	ds_read_b128 v[138:141], v207 offset:0x500
	ds_read_b128 v[142:145], v207 offset:0xa00
	ds_read_b128 v[146:149], v207 offset:0xf00
	s_waitcnt lgkmcnt(8)
	v_mfma_scale_f32_16x16x128_f8f6f4 v[88:91], v[92:99], v[0:7], v[210:213], v178, v177 op_sel_hi:[0,0,0]
	s_waitcnt lgkmcnt(6)
	v_mfma_scale_f32_16x16x128_f8f6f4 v[92:95], v[118:125], v[0:7], v[210:213], v178, v177 op_sel_hi:[0,0,0]
	s_waitcnt lgkmcnt(4)
	v_mfma_scale_f32_16x16x128_f8f6f4 v[96:99], v[126:133], v[0:7], v[210:213], v178, v177 op_sel_hi:[0,0,0]
	ds_read_b128 v[118:121], v207 offset:0x1400
	ds_read_b128 v[122:125], v207 offset:0x1900
	ds_read_b128 v[126:129], v207 offset:0x1e00
	ds_read_b128 v[130:133], v207 offset:0x2300
	s_cmp_eq_u32 s44, s58
	s_cbranch_scc1 .Lsel_diag_g0

; __device__ __forceinline__ unsigned lds_addr(const LAS void* p) { return (unsigned)(size_t)p; }
; #define RD16(dst, base, off) asm volatile("ds_read_b128 %0, %1 offset:%2" : "=&v"(dst) : "v"(base), "i"(off) : "memory")
; #define LGKM_W(n) asm volatile("s_waitcnt lgkmcnt(" #n ")" ::: "memory"); SBAR()
; #define QK8_MM(T_) do { i32x8a kf; kf.lo = lo[T_]; kf.hi = hi[T_]; s[T_] = __builtin_amdgcn_mfma_scale_f32_16x16x128_f8f6f4(kf, g.q8, (f32x4){c0, c0, c0, c0}, 0, 0, 0, 0x7f7f7f7f, 0, 0x7c7c7c7c); } while (0)
; __device__ __forceinline__ void qk8_tile_c(f32x4 (&s)[4], const GS8& g, const unsigned kb  , const float c0  ) {
;     i32x4a lo[4], hi[4];
;     RD16(lo[0], kb, 0); RD16(hi[0], kb, 16); RD16(lo[1], kb, 16 * K8ST); RD16(hi[1], kb, 16 * K8ST + 16);
;     RD16(lo[2], kb, 32 * K8ST); RD16(hi[2], kb, 32 * K8ST + 16); RD16(lo[3], kb, 48 * K8ST); RD16(hi[3], kb, 48 * K8ST + 16);
;     ...
;     LGKM_W(6); QK8_MM(0); LGKM_W(4); QK8_MM(1); LGKM_W(2); QK8_MM(2); LGKM_W(0); QK8_MM(3);
;     ...
; }
; template <bool DUMMY> __device__ __forceinline__ void sel_phase(Frame& F) {
;     ...
;                 if (a1 != 0u) {
;                     const float rf = sm8_ref(g1);
;                     VT8Frag vf; qk8_tile_c(s0, g1, lds_addr(sb) + (unsigned)klane, bB + (5.f - rf)); pv8_issue(vf, lds_addr(sb + K8TB) + (unsigned)vtlane);
.Lsel_g1_pre:
	s_lshr_b32 s45, s45, 4
	v_and_b32_e32 v18, s45, v154
	v_cmp_eq_u32_e32 vcc, 0, v18
	s_lshr_b32 s44, s66, s36
	s_and_b32 s44, s44, 0xff
	v_cndmask_b32_e32 v210, v220, v181, vcc
	v_mov_b32_e32 v211, v210
	v_mov_b32_e32 v212, v210
	v_mov_b32_e32 v213, v210
	ds_read_b128 v[126:129], v208 offset:0x1b00
	ds_read_b128 v[130:133], v208 offset:0x1b10
	s_bitcmp1_b32 s99, s37
	s_cbranch_scc1 .Lsel_qk_dma_g1
	s_waitcnt lgkmcnt(6)
	v_mfma_scale_f32_16x16x128_f8f6f4 v[84:87], v[84:91], v[8:15], v[210:213], v178, v177 op_sel_hi:[0,0,0]
	ds_read_b128 v[134:137], v207 offset:0
	ds_read_b128 v[138:141], v207 offset:0x500
	ds_read_b128 v[142:145], v207 offset:0xa00
	ds_read_b128 v[146:149], v207 offset:0xf00
	s_waitcnt lgkmcnt(8)
	v_mfma_scale_f32_16x16x128_f8f6f4 v[88:91], v[92:99], v[8:15], v[210:213], v178, v177 op_sel_hi:[0,0,0]
	s_waitcnt lgkmcnt(6)
	v_mfma_scale_f32_16x16x128_f8f6f4 v[92:95], v[118:125], v[8:15], v[210:213], v178, v177 op_sel_hi:[0,0,0]
	s_waitcnt lgkmcnt(4)
	v_mfma_scale_f32_16x16x128_f8f6f4 v[96:99], v[126:133], v[8:15], v[210:213], v178, v177 op_sel_hi:[0,0,0]
	ds_read_b128 v[118:121], v207 offset:0x1400
	ds_read_b128 v[122:125], v207 offset:0x1900
	ds_read_b128 v[126:129], v207 offset:0x1e00
	ds_read_b128 v[130:133], v207 offset:0x2300
	s_cmp_eq_u32 s44, s58
	s_cbranch_scc1 .Lsel_diag_g1

; #define LAS __attribute__((address_space(3)))
; #define RD16(dst, base, off) asm volatile("ds_read_b128 %0, %1 offset:%2" : "=&v"(dst) : "v"(base), "i"(off) : "memory")
; #define LGKM_W(n) asm volatile("s_waitcnt lgkmcnt(" #n ")" ::: "memory"); SBAR()
; #define QK8_MM(T_) do { i32x8a kf; kf.lo = lo[T_]; kf.hi = hi[T_]; s[T_] = __builtin_amdgcn_mfma_scale_f32_16x16x128_f8f6f4(kf, g.q8, (f32x4){c0, c0, c0, c0}, 0, 0, 0, 0x7f7f7f7f, 0, 0x7c7c7c7c); } while (0)
; __device__ __forceinline__ void ringS_dma(const RingSLane& R, const char* K8p, const char* VTp, LAS unsigned char* sb, int wave) {
;     __builtin_amdgcn_global_load_lds((const unsigned*)(K8p + R.so[0]), (LAS unsigned*)(sb + wave * 1024), 16, 0, 0);
;     __builtin_amdgcn_global_load_lds((const unsigned*)((wave == 0 ? K8p : VTp) + R.so[1]), (LAS unsigned*)(sb + (wave + 8) * 1024), 16, 0, 0);
;     if (wave <= 2) __builtin_amdgcn_global_load_lds((const unsigned*)(VTp + R.so[2]), (LAS unsigned*)(sb + (wave + 16) * 1024), 16, 0, 0);
; }
; __device__ __forceinline__ void qk8_tile_c(f32x4 (&s)[4], const GS8& g, const unsigned kb  , const float c0  ) {
;     i32x4a lo[4], hi[4];
;     RD16(lo[0], kb, 0); RD16(hi[0], kb, 16); RD16(lo[1], kb, 16 * K8ST); RD16(hi[1], kb, 16 * K8ST + 16);
;     RD16(lo[2], kb, 32 * K8ST); RD16(hi[2], kb, 32 * K8ST + 16); RD16(lo[3], kb, 48 * K8ST); RD16(hi[3], kb, 48 * K8ST + 16);
;     ...
;     LGKM_W(6); QK8_MM(0); LGKM_W(4); QK8_MM(1); LGKM_W(2); QK8_MM(2); LGKM_W(0); QK8_MM(3);
;     ...
; }
.Lsel_qk_dma_g0:
	s_waitcnt lgkmcnt(6)
	v_mfma_scale_f32_16x16x128_f8f6f4 v[84:87], v[84:91], v[0:7], v[210:213], v178, v177 op_sel_hi:[0,0,0]
	ds_read_b128 v[134:137], v207 offset:0
	ds_read_b128 v[138:141], v207 offset:0x500
	ds_read_b128 v[142:145], v207 offset:0xa00
	ds_read_b128 v[146:149], v207 offset:0xf00
	s_lshr_b32 vcc_lo, s60, s36
	s_and_b32 vcc_lo, vcc_lo, 0xff
	s_lshl_b32 vcc_lo, vcc_lo, 13
	s_add_u32 s12, s62, vcc_lo
	s_addc_u32 s13, s63, 0
	s_add_u32 s100, s64, vcc_lo
	s_addc_u32 s101, s65, 0
	s_mul_i32 vcc_hi, s37, 0x4c00
	s_add_i32 vcc_hi, s98, vcc_hi
	s_waitcnt lgkmcnt(8)
	v_mfma_scale_f32_16x16x128_f8f6f4 v[88:91], v[92:99], v[0:7], v[210:213], v178, v177 op_sel_hi:[0,0,0]
	s_mov_b32 m0, vcc_hi
	s_cmp_lg_u64 s[16:17], 0
	global_load_lds_dwordx4 v102, s[12:13]
	s_cselect_b32 s13, s13, s101
	s_cselect_b32 s12, s12, s100
	s_add_i32 m0, vcc_hi, 0x2000
	s_cmp_lg_u64 s[10:11], 0
	s_waitcnt lgkmcnt(6)
	v_mfma_scale_f32_16x16x128_f8f6f4 v[92:95], v[118:125], v[0:7], v[210:213], v178, v177 op_sel_hi:[0,0,0]
	global_load_lds_dwordx4 v106, s[12:13]
	s_bitset0_b32 s99, s37
	s_cbranch_scc1 .Lsel_qk_s3_g0
	s_add_i32 m0, vcc_hi, 0x4000
	s_nop 0
	global_load_lds_dwordx4 v108, s[100:101]
.Lsel_qk_s3_g0:
	s_waitcnt lgkmcnt(4)
	v_mfma_scale_f32_16x16x128_f8f6f4 v[96:99], v[126:133], v[0:7], v[210:213], v178, v177 op_sel_hi:[0,0,0]
	ds_read_b128 v[118:121], v207 offset:0x1400
	ds_read_b128 v[122:125], v207 offset:0x1900
	ds_read_b128 v[126:129], v207 offset:0x1e00
	ds_read_b128 v[130:133], v207 offset:0x2300
	s_cmp_eq_u32 s44, s58
	s_cbranch_scc1 .Lsel_diag_g0
	s_branch .LBB0_1806
.Lsel_qk_dma_g1:
	s_waitcnt lgkmcnt(6)
	v_mfma_scale_f32_16x16x128_f8f6f4 v[84:87], v[84:91], v[8:15], v[210:213], v178, v177 op_sel_hi:[0,0,0]
	ds_read_b128 v[134:137], v207 offset:0
	ds_read_b128 v[138:141], v207 offset:0x500
	ds_read_b128 v[142:145], v207 offset:0xa00
	ds_read_b128 v[146:149], v207 offset:0xf00
	s_lshr_b32 vcc_lo, s60, s36
	s_and_b32 vcc_lo, vcc_lo, 0xff
	s_lshl_b32 vcc_lo, vcc_lo, 13
	s_add_u32 s12, s62, vcc_lo
	s_addc_u32 s13, s63, 0
	s_add_u32 s100, s64, vcc_lo
	s_addc_u32 s101, s65, 0
	s_mul_i32 vcc_hi, s37, 0x4c00
	s_add_i32 vcc_hi, s98, vcc_hi
	s_waitcnt lgkmcnt(8)
	v_mfma_scale_f32_16x16x128_f8f6f4 v[88:91], v[92:99], v[8:15], v[210:213], v178, v177 op_sel_hi:[0,0,0]
	s_mov_b32 m0, vcc_hi
	s_cmp_lg_u64 s[16:17], 0
	global_load_lds_dwordx4 v102, s[12:13]
	s_cselect_b32 s13, s13, s101
	s_cselect_b32 s12, s12, s100
	s_add_i32 m0, vcc_hi, 0x2000
	s_cmp_lg_u64 s[10:11], 0
	s_waitcnt lgkmcnt(6)
	v_mfma_scale_f32_16x16x128_f8f6f4 v[92:95], v[118:125], v[8:15], v[210:213], v178, v177 op_sel_hi:[0,0,0]
	global_load_lds_dwordx4 v106, s[12:13]
	s_bitset0_b32 s99, s37
	s_cbranch_scc1 .Lsel_qk_s3_g1
	s_add_i32 m0, vcc_hi, 0x4000
	s_nop 0
	global_load_lds_dwordx4 v108, s[100:101]
.Lsel_qk_s3_g1:
	s_waitcnt lgkmcnt(4)
	v_mfma_scale_f32_16x16x128_f8f6f4 v[96:99], v[126:133], v[8:15], v[210:213], v178, v177 op_sel_hi:[0,0,0]
	ds_read_b128 v[118:121], v207 offset:0x1400
	ds_read_b128 v[122:125], v207 offset:0x1900
	ds_read_b128 v[126:129], v207 offset:0x1e00
	ds_read_b128 v[130:133], v207 offset:0x2300
	s_cmp_eq_u32 s44, s58
	s_cbranch_scc1 .Lsel_diag_g1
	s_branch .LBB0_1812
